# P8 top-4: in-row max reductions by DPP, one ds_bpermute per reduction instead of five (on top of the MoBA near-tile bias rewrite)
# baseline (speedup 1.0000x reference)
; #define LAS __attribute__((address_space(3)))
; __global__ void __launch_bounds__(512, 2) mega_fwd(Args args) {
;     ...
;             { f32x4 a0 = {0.f, 0.f, 0.f, 0.f}, a1 = {0.f, 0.f, 0.f, 0.f};
;               const int aoffs = (lane & 15) * AST + (wave * 256 + (lane >> 4) * 8) * 2;
; #pragma unroll
;               for (int ks = 0; ks < 8; ++ks) { const bf16x8 xh = *(const LAS bf16x8*)(Ahi + aoffs + ks * 64), xl = *(const LAS bf16x8*)(Alo + aoffs + ks * 64);
;                   a0 = __builtin_amdgcn_mfma_f32_16x16x32_bf16(xh, bh[0][ks], a0, 0, 0, 0); a1 = __builtin_amdgcn_mfma_f32_16x16x32_bf16(xh, bh[1][ks], a1, 0, 0, 0);
;                   a0 = __builtin_amdgcn_mfma_f32_16x16x32_bf16(xh, bl[0][ks], a0, 0, 0, 0); a1 = __builtin_amdgcn_mfma_f32_16x16x32_bf16(xh, bl[1][ks], a1, 0, 0, 0);
;                   a0 = __builtin_amdgcn_mfma_f32_16x16x32_bf16(xl, bh[0][ks], a0, 0, 0, 0); a1 = __builtin_amdgcn_mfma_f32_16x16x32_bf16(xl, bh[1][ks], a1, 0, 0, 0); }
; #pragma unroll
;               for (int rg = 0; rg < 4; ++rg) { LAS float* pp = part + (wave * 16 + (lane >> 4) * 4 + rg) * 32 + (lane & 15); pp[0] = a0[rg]; pp[16] = a1[rg]; } }
;             __syncthreads();
.LBB0_1998:
	s_waitcnt lgkmcnt(0)
	s_barrier
	ds_read_b128 v[212:215], v203
	ds_read_b128 v[216:219], v203 offset:64
	s_waitcnt lgkmcnt(1)
	v_mfma_f32_16x16x32_bf16 v[220:223], v[212:215], v[2:5], 0
	v_add_u32_e32 v192, 0x10100, v203
	v_mfma_f32_16x16x32_bf16 v[224:227], v[212:215], v[66:69], 0
	v_mfma_f32_16x16x32_bf16 v[220:223], v[212:215], v[6:9], v[220:223]
	v_mfma_f32_16x16x32_bf16 v[212:215], v[212:215], v[70:73], v[224:227]
	s_nop 5
	ds_read_b128 v[224:227], v192
	ds_read_b128 v[228:231], v192 offset:64
	s_waitcnt lgkmcnt(1)
	v_mfma_f32_16x16x32_bf16 v[220:223], v[224:227], v[2:5], v[220:223]
	v_mfma_f32_16x16x32_bf16 v[212:215], v[224:227], v[66:69], v[212:215]
	v_mfma_f32_16x16x32_bf16 v[220:223], v[216:219], v[10:13], v[220:223]
	v_mfma_f32_16x16x32_bf16 v[212:215], v[216:219], v[74:77], v[212:215]
	v_mfma_f32_16x16x32_bf16 v[220:223], v[216:219], v[14:17], v[220:223]
	v_mfma_f32_16x16x32_bf16 v[212:215], v[216:219], v[78:81], v[212:215]
	s_waitcnt lgkmcnt(0)
	v_mfma_f32_16x16x32_bf16 v[216:219], v[228:231], v[10:13], v[220:223]
	s_nop 4
	ds_read_b128 v[220:223], v203 offset:128
	ds_read_b128 v[224:227], v203 offset:192
	v_mfma_f32_16x16x32_bf16 v[212:215], v[228:231], v[74:77], v[212:215]
	s_waitcnt lgkmcnt(1)
	v_mfma_f32_16x16x32_bf16 v[216:219], v[220:223], v[18:21], v[216:219]
	v_mfma_f32_16x16x32_bf16 v[212:215], v[220:223], v[82:85], v[212:215]
	v_mfma_f32_16x16x32_bf16 v[216:219], v[220:223], v[22:25], v[216:219]
	v_mfma_f32_16x16x32_bf16 v[212:215], v[220:223], v[86:89], v[212:215]
	ds_read_b128 v[220:223], v192 offset:128
	ds_read_b128 v[228:231], v192 offset:192
	s_waitcnt lgkmcnt(1)
	v_mfma_f32_16x16x32_bf16 v[216:219], v[220:223], v[18:21], v[216:219]
	v_mfma_f32_16x16x32_bf16 v[212:215], v[220:223], v[82:85], v[212:215]
	v_mfma_f32_16x16x32_bf16 v[216:219], v[224:227], v[26:29], v[216:219]
	v_mfma_f32_16x16x32_bf16 v[212:215], v[224:227], v[90:93], v[212:215]
	v_mfma_f32_16x16x32_bf16 v[216:219], v[224:227], v[30:33], v[216:219]
	v_mfma_f32_16x16x32_bf16 v[212:215], v[224:227], v[94:97], v[212:215]
	ds_read_b128 v[220:223], v203 offset:256
	ds_read_b128 v[224:227], v203 offset:320
	s_waitcnt lgkmcnt(2)
	v_mfma_f32_16x16x32_bf16 v[216:219], v[228:231], v[26:29], v[216:219]
	v_mfma_f32_16x16x32_bf16 v[212:215], v[228:231], v[90:93], v[212:215]
	s_waitcnt lgkmcnt(1)
	v_mfma_f32_16x16x32_bf16 v[216:219], v[220:223], v[34:37], v[216:219]
	v_mfma_f32_16x16x32_bf16 v[212:215], v[220:223], v[98:101], v[212:215]
	v_mfma_f32_16x16x32_bf16 v[216:219], v[220:223], v[38:41], v[216:219]
	v_mfma_f32_16x16x32_bf16 v[212:215], v[220:223], v[102:105], v[212:215]
	ds_read_b128 v[220:223], v192 offset:256
	ds_read_b128 v[228:231], v192 offset:320
	s_waitcnt lgkmcnt(1)
	v_mfma_f32_16x16x32_bf16 v[216:219], v[220:223], v[34:37], v[216:219]
	v_mfma_f32_16x16x32_bf16 v[212:215], v[220:223], v[98:101], v[212:215]
	v_mfma_f32_16x16x32_bf16 v[216:219], v[224:227], v[42:45], v[216:219]
	v_mfma_f32_16x16x32_bf16 v[212:215], v[224:227], v[106:109], v[212:215]
	v_mfma_f32_16x16x32_bf16 v[216:219], v[224:227], v[46:49], v[216:219]
	v_mfma_f32_16x16x32_bf16 v[212:215], v[224:227], v[110:113], v[212:215]
	ds_read_b128 v[220:223], v203 offset:384
	ds_read_b128 v[224:227], v203 offset:448
	s_waitcnt lgkmcnt(2)
	v_mfma_f32_16x16x32_bf16 v[216:219], v[228:231], v[42:45], v[216:219]
	v_mfma_f32_16x16x32_bf16 v[212:215], v[228:231], v[106:109], v[212:215]
	s_waitcnt lgkmcnt(1)
	v_mfma_f32_16x16x32_bf16 v[216:219], v[220:223], v[50:53], v[216:219]
	v_mfma_f32_16x16x32_bf16 v[212:215], v[220:223], v[114:117], v[212:215]
	v_mfma_f32_16x16x32_bf16 v[216:219], v[220:223], v[54:57], v[216:219]
	v_mfma_f32_16x16x32_bf16 v[212:215], v[220:223], v[118:121], v[212:215]
	ds_read_b128 v[220:223], v192 offset:384
	ds_read_b128 v[228:231], v192 offset:448
	s_waitcnt lgkmcnt(1)
	v_mfma_f32_16x16x32_bf16 v[216:219], v[220:223], v[50:53], v[216:219]
	v_mfma_f32_16x16x32_bf16 v[212:215], v[220:223], v[114:117], v[212:215]
	v_mfma_f32_16x16x32_bf16 v[216:219], v[224:227], v[58:61], v[216:219]
	v_mfma_f32_16x16x32_bf16 v[212:215], v[224:227], v[122:125], v[212:215]
	v_mfma_f32_16x16x32_bf16 v[216:219], v[224:227], v[62:65], v[216:219]
	v_mfma_f32_16x16x32_bf16 v[212:215], v[224:227], v[126:129], v[212:215]
	s_waitcnt lgkmcnt(0)
	v_mfma_f32_16x16x32_bf16 v[216:219], v[228:231], v[58:61], v[216:219]
	v_mfma_f32_16x16x32_bf16 v[212:215], v[228:231], v[122:125], v[212:215]
	s_nop 7
	ds_write2_b32 v204, v216, v212 offset1:16
	ds_write2_b32 v204, v217, v213 offset0:32 offset1:48
	ds_write2_b32 v204, v218, v214 offset0:64 offset1:80
	ds_write2_b32 v204, v219, v215 offset0:96 offset1:112
	s_waitcnt lgkmcnt(0)
	s_barrier
	s_and_saveexec_b64 s[52:53], s[4:5]
	s_cbranch_execz .LBB0_1995
; __global__ void __launch_bounds__(512, 2) mega_fwd(Args args) {
;     ...
;             if ((tid >> 5) < CR) { const int row = tid >> 5, e = tid & 31; float x = br[e];
; #pragma unroll
;               for (int w2 = 0; w2 < 8; ++w2) x += part[(w2 * 16 + row) * 32 + e];
;               float t0 = 0.f, t1 = 0.f, t2 = 0.f, t3 = 0.f; int i0 = 0, i1 = 0, i2 = 0, i3 = 0;
; #pragma unroll
;               for (int k = 0; k < 4; ++k) { float mx = x;
; #pragma unroll
;                   for (int o = 1; o < 32; o <<= 1) mx = fmaxf(mx, __shfl_xor(mx, o));
;                   const unsigned long long bal = __ballot(x == mx); const unsigned hm = (unsigned)(bal >> (lane & 32)); const int idx = __ffs(hm) - 1;
;                   if (k == 0) { t0 = mx; i0 = idx; } else if (k == 1) { t1 = mx; i1 = idx; } else if (k == 2) { t2 = mx; i2 = idx; } else { t3 = mx; i3 = idx; }
;                   if (e == idx) x = -__builtin_inff(); }
;               const float e1 = __expf(t1 - t0), e2 = __expf(t2 - t0), e3 = __expf(t3 - t0), inv = 1.0f / (1.0f + e1 + e2 + e3);
;               if (e < 4) { const int ex = e == 0 ? i0 : (e == 1 ? i1 : (e == 2 ? i2 : i3)); const float wgt = (e == 0 ? 1.0f : (e == 1 ? e1 : (e == 2 ? e2 : e3))) * inv;
;                   const int tok = ch * CR + row; const int pos = (int)atomicAdd(ctl + CW_CNT + 64 * ex, 1u);
;                   AE[tok * 4 + e] = ex; AP[tok * 4 + e] = pos; AW[tok * 4 + e] = wgt; LIST[ex * T + pos] = tok; } }
	v_mbcnt_lo_u32_b32 v253, -1, 0
	v_mbcnt_hi_u32_b32 v253, -1, v253
	v_xor_b32_e32 v253, 16, v253
	v_lshlrev_b32_e32 v253, 2, v253
	global_load_dword v192, v[176:177], off
	ds_read2st64_b32 v[194:195], v165 offset1:8
	ds_read2st64_b32 v[212:213], v165 offset0:16 offset1:24
	ds_read2st64_b32 v[214:215], v165 offset0:32 offset1:40
	ds_read2st64_b32 v[216:217], v165 offset0:48 offset1:56
	s_waitcnt vmcnt(0) lgkmcnt(3)
	v_add_f32_e32 v192, v192, v194
	v_add_f32_e32 v192, v192, v195
	s_waitcnt lgkmcnt(2)
	v_add_f32_e32 v192, v192, v212
	v_add_f32_e32 v192, v192, v213
	s_waitcnt lgkmcnt(1)
	v_add_f32_e32 v192, v192, v214
	v_add_f32_e32 v192, v192, v215
	s_waitcnt lgkmcnt(0)
	v_add_f32_e32 v192, v192, v216
	v_add_f32_e32 v211, v192, v217
	s_nop 1
	v_max_f32_dpp v192, v211, v211 quad_perm:[1,0,3,2] row_mask:0xf bank_mask:0xf
	s_nop 1
	v_max_f32_dpp v192, v192, v192 quad_perm:[2,3,0,1] row_mask:0xf bank_mask:0xf
	s_nop 1
	v_max_f32_dpp v192, v192, v192 row_half_mirror row_mask:0xf bank_mask:0xf
	s_nop 1
	v_max_f32_dpp v192, v192, v192 row_mirror row_mask:0xf bank_mask:0xf
	s_nop 0
	ds_bpermute_b32 v194, v253, v192
	s_waitcnt lgkmcnt(0)
	v_max_f32_e32 v192, v192, v194
	v_cmp_eq_f32_e32 vcc, v211, v192
	s_nop 1
	v_lshrrev_b64 v[194:195], v178, vcc
	v_ffbl_b32_e32 v194, v194
	v_cmp_ne_u32_e32 vcc, v163, v194
	s_nop 1
	v_cndmask_b32_e32 v214, v207, v211, vcc
	s_nop 1
	v_max_f32_dpp v195, v214, v214 quad_perm:[1,0,3,2] row_mask:0xf bank_mask:0xf
	s_nop 1
	v_max_f32_dpp v195, v195, v195 quad_perm:[2,3,0,1] row_mask:0xf bank_mask:0xf
	s_nop 1
	v_max_f32_dpp v195, v195, v195 row_half_mirror row_mask:0xf bank_mask:0xf
	s_nop 1
	v_max_f32_dpp v195, v195, v195 row_mirror row_mask:0xf bank_mask:0xf
	s_nop 0
	ds_bpermute_b32 v211, v253, v195
	s_waitcnt lgkmcnt(0)
	v_max_f32_e32 v195, v195, v211
	v_cmp_eq_f32_e32 vcc, v214, v195
	s_nop 1
	v_lshrrev_b64 v[212:213], v178, vcc
	v_ffbl_b32_e32 v211, v212
	v_cmp_ne_u32_e32 vcc, v163, v211
	s_nop 1
	v_cndmask_b32_e32 v216, v207, v214, vcc
	s_nop 1
	v_max_f32_dpp v212, v216, v216 quad_perm:[1,0,3,2] row_mask:0xf bank_mask:0xf
	s_nop 1
	v_max_f32_dpp v212, v212, v212 quad_perm:[2,3,0,1] row_mask:0xf bank_mask:0xf
	s_nop 1
	v_max_f32_dpp v212, v212, v212 row_half_mirror row_mask:0xf bank_mask:0xf
	s_nop 1
	v_max_f32_dpp v212, v212, v212 row_mirror row_mask:0xf bank_mask:0xf
	s_nop 0
	ds_bpermute_b32 v213, v253, v212
	s_waitcnt lgkmcnt(0)
	v_max_f32_e32 v212, v212, v213
	v_cmp_eq_f32_e32 vcc, v216, v212
	s_nop 1
	v_lshrrev_b64 v[214:215], v178, vcc
	v_ffbl_b32_e32 v213, v214
	v_cmp_ne_u32_e32 vcc, v163, v213
	s_nop 1
	v_cndmask_b32_e32 v214, v207, v216, vcc
	s_nop 1
	v_max_f32_dpp v191, v214, v214 quad_perm:[1,0,3,2] row_mask:0xf bank_mask:0xf
	s_nop 1
	v_max_f32_dpp v191, v191, v191 quad_perm:[2,3,0,1] row_mask:0xf bank_mask:0xf
	s_nop 1
	v_max_f32_dpp v191, v191, v191 row_half_mirror row_mask:0xf bank_mask:0xf
	s_nop 1
	v_max_f32_dpp v191, v191, v191 row_mirror row_mask:0xf bank_mask:0xf
	s_nop 0
	ds_bpermute_b32 v193, v253, v191
	s_waitcnt lgkmcnt(0)
	v_max_f32_e32 v191, v191, v193
	v_cmp_eq_f32_e32 vcc, v214, v191
	s_and_b64 exec, exec, s[6:7]
	s_cbranch_execz .LBB0_1995
	v_lshrrev_b64 v[208:209], v178, vcc
	v_ffbl_b32_e32 v193, v208
	v_cndmask_b32_e64 v193, v193, v213, s[12:13]
	v_cndmask_b32_e64 v193, v193, v211, s[10:11]
	v_cndmask_b32_e64 v210, v193, v194, s[8:9]
	v_lshlrev_b32_e32 v208, 6, v210
	v_ashrrev_i32_e32 v209, 31, v208
	v_lshl_add_u64 v[208:209], v[208:209], 2, s[50:51]
	global_atomic_add v211, v[208:209], v205, off sc0
	v_sub_f32_e32 v193, v195, v192
	v_sub_f32_e32 v194, v212, v192
	v_sub_f32_e32 v192, v191, v192
	v_ashrrev_i32_e32 v191, 31, v190
	v_mul_f32_e32 v195, 0x3fb8aa3b, v193
	v_mul_f32_e32 v194, 0x3fb8aa3b, v194
	v_mul_f32_e32 v208, 0x3fb8aa3b, v192
	v_lshlrev_b64 v[192:193], 2, v[190:191]
	v_exp_f32_e32 v191, v195
	v_exp_f32_e32 v213, v194
	v_exp_f32_e32 v214, v208
	v_lshl_add_u64 v[194:195], s[42:43], 0, v[192:193]
	v_add_f32_e32 v215, 1.0, v191
	global_store_dword v[194:195], v210, off
	v_cndmask_b32_e64 v216, v214, v213, s[12:13]
	v_add_f32_e32 v213, v213, v215
	v_add_f32_e32 v213, v214, v213
	v_div_scale_f32 v214, s[56:57], v213, v213, 1.0
	v_rcp_f32_e32 v215, v214
	v_div_scale_f32 v194, vcc, 1.0, v213, 1.0
	v_cndmask_b32_e64 v191, v216, v191, s[10:11]
	v_fma_f32 v195, -v214, v215, 1.0
	v_fmac_f32_e32 v215, v195, v215
	v_mul_f32_e32 v195, v194, v215
	v_fma_f32 v216, -v214, v195, v194
	v_fmac_f32_e32 v195, v216, v215
	v_fma_f32 v194, -v214, v195, v194
	v_div_fmas_f32 v194, v194, v215, v195
	v_cndmask_b32_e64 v191, v191, 1.0, s[8:9]
	v_div_fixup_f32 v194, v194, v213, 1.0
	v_lshl_add_u64 v[208:209], s[44:45], 0, v[192:193]
	v_lshl_add_u64 v[192:193], s[46:47], 0, v[192:193]
	v_mul_f32_e32 v191, v191, v194
	v_add_u32_e32 v212, s3, v1
	global_store_dword v[192:193], v191, off
	s_waitcnt vmcnt(2)
	global_store_dword v[208:209], v211, off
	v_lshl_add_u32 v192, v210, 14, v211
	v_ashrrev_i32_e32 v193, 31, v192
	v_lshl_add_u64 v[192:193], v[192:193], 2, s[48:49]
	global_store_dword v[192:193], v212, off
	s_branch .LBB0_1995
